# speedup vs baseline: 1.0746x; 1.0139x over previous
.LBB7_38:
	s_or_b64 exec, exec, s[0:1]
	s_lshl_b64 s[0:1], s[6:7], 2
	s_waitcnt lgkmcnt(0)
	s_add_u32 s4, s8, s0
	s_addc_u32 s5, s9, s1
	s_lshl_b32 s10, s6, 12
	s_waitcnt vmcnt(0)
	v_cmp_ne_u32_e32 vcc, 0, v15
	v_lshrrev_b32_e32 v17, 19, v15
	v_cmp_ge_i32_e64 s[12:13], v17, v16
	s_and_b64 s[20:21], vcc, s[12:13]
	s_bcnt1_i32_b64 s40, s[20:21]
	v_cmp_ne_u32_e32 vcc, 0, v13
	v_lshrrev_b32_e32 v17, 19, v13
	v_cmp_ge_i32_e64 s[12:13], v17, v16
	s_and_b64 s[22:23], vcc, s[12:13]
	s_bcnt1_i32_b64 s41, s[22:23]
	v_cmp_ne_u32_e32 vcc, 0, v11
	v_lshrrev_b32_e32 v17, 19, v11
	v_cmp_ge_i32_e64 s[12:13], v17, v16
	s_and_b64 s[24:25], vcc, s[12:13]
	s_bcnt1_i32_b64 s42, s[24:25]
	v_cmp_ne_u32_e32 vcc, 0, v9
	v_lshrrev_b32_e32 v17, 19, v9
	v_cmp_ge_i32_e64 s[12:13], v17, v16
	s_and_b64 s[26:27], vcc, s[12:13]
	s_bcnt1_i32_b64 s43, s[26:27]
	v_cmp_ne_u32_e32 vcc, 0, v7
	v_lshrrev_b32_e32 v17, 19, v7
	v_cmp_ge_i32_e64 s[12:13], v17, v16
	s_and_b64 s[28:29], vcc, s[12:13]
	s_bcnt1_i32_b64 s44, s[28:29]
	v_cmp_ne_u32_e32 vcc, 0, v5
	v_lshrrev_b32_e32 v17, 19, v5
	v_cmp_ge_i32_e64 s[12:13], v17, v16
	s_and_b64 s[30:31], vcc, s[12:13]
	s_bcnt1_i32_b64 s45, s[30:31]
	v_cmp_ne_u32_e32 vcc, 0, v3
	v_lshrrev_b32_e32 v17, 19, v3
	v_cmp_ge_i32_e64 s[12:13], v17, v16
	s_and_b64 s[32:33], vcc, s[12:13]
	s_bcnt1_i32_b64 s46, s[32:33]
	v_cmp_ne_u32_e32 vcc, 0, v1
	v_lshrrev_b32_e32 v17, 19, v1
	v_cmp_ge_i32_e64 s[12:13], v17, v16
	s_and_b64 s[34:35], vcc, s[12:13]
	s_bcnt1_i32_b64 s47, s[34:35]
	s_add_i32 s11, s40, s41
	s_add_i32 s11, s11, s42
	s_add_i32 s11, s11, s43
	s_add_i32 s11, s11, s44
	s_add_i32 s11, s11, s45
	s_add_i32 s11, s11, s46
	s_add_i32 s11, s11, s47
	v_readfirstlane_b32 s12, v14
	s_bfe_u32 s12, s12, 0x30006
	s_lshl_b32 s13, s12, 2
	v_mov_b32_e32 v17, s11
	v_mov_b32_e32 v18, s13
	s_mov_b64 exec, 1
	ds_write_b32 v18, v17
	s_mov_b64 exec, -1
	s_waitcnt lgkmcnt(0)
	s_barrier
	v_mov_b32_e32 v18, 0
	ds_read_b128 v[20:23], v18
	ds_read_b128 v[24:27], v18 offset:16
	s_waitcnt lgkmcnt(0)
	v_readfirstlane_b32 s48, v20
	v_readfirstlane_b32 s49, v21
	v_readfirstlane_b32 s50, v22
	v_readfirstlane_b32 s51, v23
	v_readfirstlane_b32 s52, v24
	v_readfirstlane_b32 s53, v25
	v_readfirstlane_b32 s54, v26
	v_readfirstlane_b32 s55, v27
	s_mov_b32 s14, 0
	s_mov_b32 s16, 0
	s_cmp_lt_u32 0, s12
	s_cselect_b32 s17, s48, 0
	s_add_i32 s14, s14, s17
	s_add_i32 s16, s16, s48
	s_cmp_lt_u32 1, s12
	s_cselect_b32 s17, s49, 0
	s_add_i32 s14, s14, s17
	s_add_i32 s16, s16, s49
	s_cmp_lt_u32 2, s12
	s_cselect_b32 s17, s50, 0
	s_add_i32 s14, s14, s17
	s_add_i32 s16, s16, s50
	s_cmp_lt_u32 3, s12
	s_cselect_b32 s17, s51, 0
	s_add_i32 s14, s14, s17
	s_add_i32 s16, s16, s51
	s_cmp_lt_u32 4, s12
	s_cselect_b32 s17, s52, 0
	s_add_i32 s14, s14, s17
	s_add_i32 s16, s16, s52
	s_cmp_lt_u32 5, s12
	s_cselect_b32 s17, s53, 0
	s_add_i32 s14, s14, s17
	s_add_i32 s16, s16, s53
	s_cmp_lt_u32 6, s12
	s_cselect_b32 s17, s54, 0
	s_add_i32 s14, s14, s17
	s_add_i32 s16, s16, s54
	s_cmp_lt_u32 7, s12
	s_cselect_b32 s17, s55, 0
	s_add_i32 s14, s14, s17
	s_add_i32 s16, s16, s55
	s_cmp_lg_u32 s12, 0
	s_cbranch_scc1 .Lmy_collect_noatom
	s_cmp_eq_u32 s16, 0
	s_cbranch_scc1 .Lmy_collect_noatom
	v_mov_b32_e32 v17, 0
	v_mov_b32_e32 v19, s16
	s_mov_b64 exec, 1
	global_atomic_add v17, v17, v19, s[4:5] sc0
	s_waitcnt vmcnt(0)
	v_mov_b32_e32 v18, 0
	ds_write_b32 v18, v17 offset:64
	s_mov_b64 exec, -1
.Lmy_collect_noatom:
	s_waitcnt lgkmcnt(0)
	s_barrier
	s_cmp_eq_u32 s11, 0
	s_cbranch_scc1 .Lmy_collect_done
	v_mov_b32_e32 v18, 0
	ds_read_b32 v17, v18 offset:64
	s_movk_i32 s15, 0x1000
	s_waitcnt lgkmcnt(0)
	v_readfirstlane_b32 s17, v17
	s_add_i32 s14, s14, s17
	v_mbcnt_lo_u32_b32 v19, s20, 0
	v_mbcnt_hi_u32_b32 v19, s21, v19
	v_add_u32_e32 v19, s14, v19
	v_cmp_gt_i32_e32 vcc, s15, v19
	v_add_lshl_u32 v20, v19, s10, 2
	s_and_b64 exec, s[20:21], vcc
	global_store_dword v20, v14, s[2:3]
	s_mov_b64 exec, -1
	s_add_i32 s14, s14, s40
	v_mbcnt_lo_u32_b32 v19, s22, 0
	v_mbcnt_hi_u32_b32 v19, s23, v19
	v_add_u32_e32 v19, s14, v19
	v_cmp_gt_i32_e32 vcc, s15, v19
	v_add_lshl_u32 v20, v19, s10, 2
	s_and_b64 exec, s[22:23], vcc
	global_store_dword v20, v12, s[2:3]
	s_mov_b64 exec, -1
	s_add_i32 s14, s14, s41
	v_mbcnt_lo_u32_b32 v19, s24, 0
	v_mbcnt_hi_u32_b32 v19, s25, v19
	v_add_u32_e32 v19, s14, v19
	v_cmp_gt_i32_e32 vcc, s15, v19
	v_add_lshl_u32 v20, v19, s10, 2
	s_and_b64 exec, s[24:25], vcc
	global_store_dword v20, v10, s[2:3]
	s_mov_b64 exec, -1
	s_add_i32 s14, s14, s42
	v_mbcnt_lo_u32_b32 v19, s26, 0
	v_mbcnt_hi_u32_b32 v19, s27, v19
	v_add_u32_e32 v19, s14, v19
	v_cmp_gt_i32_e32 vcc, s15, v19
	v_add_lshl_u32 v20, v19, s10, 2
	s_and_b64 exec, s[26:27], vcc
	global_store_dword v20, v8, s[2:3]
	s_mov_b64 exec, -1
	s_add_i32 s14, s14, s43
	v_mbcnt_lo_u32_b32 v19, s28, 0
	v_mbcnt_hi_u32_b32 v19, s29, v19
	v_add_u32_e32 v19, s14, v19
	v_cmp_gt_i32_e32 vcc, s15, v19
	v_add_lshl_u32 v20, v19, s10, 2
	s_and_b64 exec, s[28:29], vcc
	global_store_dword v20, v6, s[2:3]
	s_mov_b64 exec, -1
	s_add_i32 s14, s14, s44
	v_mbcnt_lo_u32_b32 v19, s30, 0
	v_mbcnt_hi_u32_b32 v19, s31, v19
	v_add_u32_e32 v19, s14, v19
	v_cmp_gt_i32_e32 vcc, s15, v19
	v_add_lshl_u32 v20, v19, s10, 2
	s_and_b64 exec, s[30:31], vcc
	global_store_dword v20, v4, s[2:3]
	s_mov_b64 exec, -1
	s_add_i32 s14, s14, s45
	v_mbcnt_lo_u32_b32 v19, s32, 0
	v_mbcnt_hi_u32_b32 v19, s33, v19
	v_add_u32_e32 v19, s14, v19
	v_cmp_gt_i32_e32 vcc, s15, v19
	v_add_lshl_u32 v20, v19, s10, 2
	s_and_b64 exec, s[32:33], vcc
	global_store_dword v20, v2, s[2:3]
	s_mov_b64 exec, -1
	s_add_i32 s14, s14, s46
	v_mbcnt_lo_u32_b32 v19, s34, 0
	v_mbcnt_hi_u32_b32 v19, s35, v19
	v_add_u32_e32 v19, s14, v19
	v_cmp_gt_i32_e32 vcc, s15, v19
	v_add_lshl_u32 v20, v19, s10, 2
	s_and_b64 exec, s[34:35], vcc
	global_store_dword v20, v0, s[2:3]
	s_mov_b64 exec, -1
	s_add_i32 s14, s14, s47

	.amdhsa_kernel _Z14collect_kernelPKjS0_PiS1_
		.amdhsa_group_segment_fixed_size 2052
		.amdhsa_private_segment_fixed_size 0
		.amdhsa_kernarg_size 32
		.amdhsa_user_sgpr_count 2
		.amdhsa_user_sgpr_dispatch_ptr 0
		.amdhsa_user_sgpr_queue_ptr 0
		.amdhsa_user_sgpr_kernarg_segment_ptr 1
		.amdhsa_user_sgpr_dispatch_id 0
		.amdhsa_user_sgpr_kernarg_preload_length 0
		.amdhsa_user_sgpr_kernarg_preload_offset 0
		.amdhsa_user_sgpr_private_segment_size 0
		.amdhsa_uses_dynamic_stack 0
		.amdhsa_enable_private_segment 0
		.amdhsa_system_sgpr_workgroup_id_x 1
		.amdhsa_system_sgpr_workgroup_id_y 1
		.amdhsa_system_sgpr_workgroup_id_z 0
		.amdhsa_system_sgpr_workgroup_info 0
		.amdhsa_system_vgpr_workitem_id 0
		.amdhsa_next_free_vgpr 34
		.amdhsa_next_free_sgpr 64
		.amdhsa_accum_offset 36
		.amdhsa_reserve_vcc 1
		.amdhsa_float_round_mode_32 0
		.amdhsa_float_round_mode_16_64 0
		.amdhsa_float_denorm_mode_32 3
		.amdhsa_float_denorm_mode_16_64 3
		.amdhsa_dx10_clamp 1
		.amdhsa_ieee_mode 1
		.amdhsa_fp16_overflow 0
		.amdhsa_tg_split 0
		.amdhsa_exception_fp_ieee_invalid_op 0
		.amdhsa_exception_fp_denorm_src 0
		.amdhsa_exception_fp_ieee_div_zero 0
		.amdhsa_exception_fp_ieee_overflow 0
		.amdhsa_exception_fp_ieee_underflow 0
		.amdhsa_exception_fp_ieee_inexact 0
		.amdhsa_exception_int_div_zero 0
	.end_amdhsa_kernel

.LBB15_10:
	s_or_b64 exec, exec, s[4:5]
	v_bfe_u32 v156, v0, 6, 1
	v_lshrrev_b32_e32 v4, 1, v0
	s_load_dwordx2 s[8:9], s[0:1], 0x28
	v_and_b32_e32 v166, 31, v0
	v_lshrrev_b32_e32 v3, 5, v0
	v_lshlrev_b32_e32 v161, 6, v156
	v_and_b32_e32 v167, 0xc0, v4
	v_bfe_u32 v4, v0, 2, 2
	v_bitop3_b32 v169, v3, v4, 1 bitop3:0x6c
	v_or_b32_e32 v3, v166, v161
	v_bfe_u32 v159, v0, 5, 1
	v_lshlrev_b32_e32 v6, 2, v3
	v_mov_b32_e32 v3, 0
	v_bitop3_b32 v165, v159, v4, 2 bitop3:0x36
	v_lshl_add_u64 v[4:5], s[6:7], 0, v[2:3]
	s_mov_b64 s[0:1], 0x6000
	v_lshlrev_b32_e32 v2, 5, v0
	v_or_b32_e32 v160, 2, v159
	v_lshrrev_b32_e32 v158, 2, v0
	v_lshl_add_u64 v[150:151], v[4:5], 0, s[0:1]
	v_or_b32_e32 v170, v167, v166
	v_lshlrev_b32_e32 v171, 6, v166
	v_and_b32_e32 v172, 0x3000, v2
	s_movk_i32 s16, 0x200
	s_mov_b32 s17, 0
	v_lshlrev_b32_e32 v168, 4, v6
	s_mov_b32 s18, 0
	s_mov_b32 s19, 0
	v_mov_b32_e32 v2, 0
	v_mov_b32_e32 v4, v3
	v_mov_b32_e32 v5, v3
	v_mov_b32_e32 v6, v3
	v_mov_b32_e32 v7, v3
	v_mov_b32_e32 v8, v3
	v_mov_b32_e32 v9, v3
	v_mov_b32_e32 v10, v3
	v_mov_b32_e32 v11, v3
	v_mov_b32_e32 v12, v3
	v_mov_b32_e32 v13, v3
	v_mov_b32_e32 v14, v3
	v_mov_b32_e32 v15, v3
	v_mov_b32_e32 v16, v3
	v_mov_b32_e32 v17, v3
	v_mov_b32_e32 v18, 0
	v_mov_b32_e32 v19, v3
	v_mov_b32_e32 v20, v3
	v_mov_b32_e32 v21, v3
	v_mov_b32_e32 v22, v3
	v_mov_b32_e32 v23, v3
	v_mov_b32_e32 v24, v3
	v_mov_b32_e32 v25, v3
	v_mov_b32_e32 v26, v3
	v_mov_b32_e32 v27, v3
	v_mov_b32_e32 v28, v3
	v_mov_b32_e32 v29, v3
	v_mov_b32_e32 v30, v3
	v_mov_b32_e32 v31, v3
	v_mov_b32_e32 v32, v3
	v_mov_b32_e32 v33, v3
	v_mov_b32_e32 v50, 0
	v_mov_b32_e32 v51, v3
	v_mov_b32_e32 v52, v3
	v_mov_b32_e32 v53, v3
	v_mov_b32_e32 v54, v3
	v_mov_b32_e32 v55, v3
	v_mov_b32_e32 v56, v3
	v_mov_b32_e32 v57, v3
	v_mov_b32_e32 v58, v3
	v_mov_b32_e32 v59, v3
	v_mov_b32_e32 v60, v3
	v_mov_b32_e32 v61, v3
	v_mov_b32_e32 v62, v3
	v_mov_b32_e32 v63, v3
	v_mov_b32_e32 v64, v3
	v_mov_b32_e32 v65, v3
	v_mov_b32_e32 v82, 0
	v_mov_b32_e32 v83, v3
	v_mov_b32_e32 v84, v3
	v_mov_b32_e32 v85, v3
	v_mov_b32_e32 v86, v3
	v_mov_b32_e32 v87, v3
	v_mov_b32_e32 v88, v3
	v_mov_b32_e32 v89, v3
	v_mov_b32_e32 v90, v3
	v_mov_b32_e32 v91, v3
	v_mov_b32_e32 v92, v3
	v_mov_b32_e32 v93, v3
	v_mov_b32_e32 v94, v3
	v_mov_b32_e32 v95, v3
	v_mov_b32_e32 v96, v3
	v_mov_b32_e32 v97, v3
	v_mov_b32_e32 v34, 0
	v_mov_b32_e32 v35, v3
	v_mov_b32_e32 v36, v3
	v_mov_b32_e32 v37, v3
	v_mov_b32_e32 v38, v3
	v_mov_b32_e32 v39, v3
	v_mov_b32_e32 v40, v3
	v_mov_b32_e32 v41, v3
	v_mov_b32_e32 v42, v3
	v_mov_b32_e32 v43, v3
	v_mov_b32_e32 v44, v3
	v_mov_b32_e32 v45, v3
	v_mov_b32_e32 v46, v3
	v_mov_b32_e32 v47, v3
	v_mov_b32_e32 v48, v3
	v_mov_b32_e32 v49, v3
	v_mov_b32_e32 v66, 0
	v_mov_b32_e32 v67, v3
	v_mov_b32_e32 v68, v3
	v_mov_b32_e32 v69, v3
	v_mov_b32_e32 v70, v3
	v_mov_b32_e32 v71, v3
	v_mov_b32_e32 v72, v3
	v_mov_b32_e32 v73, v3
	v_mov_b32_e32 v74, v3
	v_mov_b32_e32 v75, v3
	v_mov_b32_e32 v76, v3
	v_mov_b32_e32 v77, v3
	v_mov_b32_e32 v78, v3
	v_mov_b32_e32 v79, v3
	v_mov_b32_e32 v80, v3
	v_mov_b32_e32 v81, v3
	v_mov_b32_e32 v98, 0
	v_mov_b32_e32 v99, v3
	v_mov_b32_e32 v100, v3
	v_mov_b32_e32 v101, v3
	v_mov_b32_e32 v102, v3
	v_mov_b32_e32 v103, v3
	v_mov_b32_e32 v104, v3
	v_mov_b32_e32 v105, v3
	v_mov_b32_e32 v106, v3
	v_mov_b32_e32 v107, v3
	v_mov_b32_e32 v108, v3
	v_mov_b32_e32 v109, v3
	v_mov_b32_e32 v110, v3
	v_mov_b32_e32 v111, v3
	v_mov_b32_e32 v112, v3
	v_mov_b32_e32 v113, v3
	v_mov_b32_e32 v114, 0
	v_mov_b32_e32 v115, v3
	v_mov_b32_e32 v116, v3
	v_mov_b32_e32 v117, v3
	v_mov_b32_e32 v118, v3
	v_mov_b32_e32 v119, v3
	v_mov_b32_e32 v120, v3
	v_mov_b32_e32 v121, v3
	v_mov_b32_e32 v122, v3
	v_mov_b32_e32 v123, v3
	v_mov_b32_e32 v124, v3
	v_mov_b32_e32 v125, v3
	v_mov_b32_e32 v126, v3
	v_mov_b32_e32 v127, v3
	v_mov_b32_e32 v128, v3
	v_mov_b32_e32 v129, v3
	s_waitcnt lgkmcnt(0)
	v_mov_b32_e32 v174, 0
	v_mov_b32_e32 v175, 0
	v_mov_b32_e32 v176, 0
	v_mov_b32_e32 v177, 0
	v_mov_b32_e32 v178, 0
	v_mov_b32_e32 v179, 0
	v_mov_b32_e32 v180, 0
	v_mov_b32_e32 v181, 0
	v_mov_b32_e32 v194, 0
	v_mov_b32_e32 v195, 0
	v_mov_b32_e32 v196, 0
	v_mov_b32_e32 v197, 0
	v_mov_b32_e32 v234, 0
	v_mov_b32_e32 v235, 0
	v_mov_b32_e32 v236, 0
	v_mov_b32_e32 v237, 0
	v_mov_b32_e32 v238, 0
	v_mov_b32_e32 v239, 0
	v_mov_b32_e32 v240, 0
	v_mov_b32_e32 v241, 0
	v_mov_b32_e32 v242, 0
	v_mov_b32_e32 v243, 0
	v_mov_b32_e32 v244, 0
	v_mov_b32_e32 v245, 0
	v_mov_b32_e32 v246, 0
	v_mov_b32_e32 v247, 0
	v_mov_b32_e32 v248, 0
	v_mov_b32_e32 v249, 0
	v_mov_b32_e32 v250, 0
	v_mov_b32_e32 v251, 0
	v_mov_b32_e32 v252, 0
	v_mov_b32_e32 v253, 0
	s_barrier
	s_branch .LBB15_13

.LBB15_13:
	v_add_co_u32_e32 v130, vcc, 0x2000, v150
	v_mov_b32_e32 v132, 0
	s_nop 0
	v_mfma_f32_32x32x16_f16 v[82:97], v[178:181], v[194:197], v[82:97]
	v_addc_co_u32_e32 v131, vcc, 0, v151, vcc
	global_load_dwordx4 v[142:145], v[150:151], off
	global_load_dwordx4 v[146:149], v[130:131], off
	v_mfma_f32_32x32x16_f16 v[114:129], v[178:181], v[234:237], v[114:129]
	v_mov_b32_e32 v130, 0
	v_mov_b32_e32 v131, 0
	v_mov_b32_e32 v133, 0
	v_mfma_f32_32x32x16_f16 v[114:129], v[246:249], v[194:197], v[114:129]
	s_and_saveexec_b64 s[4:5], s[2:3]
	s_cbranch_execz .LBB15_15
	v_add_co_u32_e32 v130, vcc, 0x4000, v150
	s_nop 1
	v_addc_co_u32_e32 v131, vcc, 0, v151, vcc
	global_load_dwordx4 v[130:133], v[130:131], off
.LBB15_15:
	s_or_b64 exec, exec, s[4:5]
	s_mul_hi_u32 s4, s19, 0xaaaaaaab
	s_lshr_b32 s23, s4, 1
	s_mul_i32 s4, s23, 0x9ba
	s_sub_i32 s20, s16, s4
	s_sub_i32 s7, s17, s4
	v_mfma_f32_32x32x16_f16 v[50:65], v[178:181], v[238:241], v[50:65]
	s_mul_i32 s4, s19, 0xab
	s_mul_i32 s5, s23, 0x8880
	s_bfe_u32 s22, s4, 0x70009
	s_add_i32 s6, s5, 0x5b00
	s_add_i32 s22, s22, 1
	v_mfma_f32_32x32x16_f16 v[98:113], v[178:181], v[242:245], v[98:113]
	s_cmp_lt_u32 s19, 21
	s_cselect_b64 s[4:5], -1, 0
	s_add_i32 s12, s7, 0x33e
	s_cmp_lg_u32 s6, s18
	s_cselect_b32 s21, s12, 0x9b8
	v_mfma_f32_32x32x16_f16 v[98:113], v[246:249], v[238:241], v[98:113]
	v_add_u32_e32 v152, s7, v0
	s_cmp_gt_u32 s19, 20
	v_mov_b32_e32 v141, 0
	v_cmp_gt_i32_e32 vcc, s21, v152
	v_mov_b32_e32 v140, 0
	v_mfma_f32_32x32x16_f16 v[18:33], v[174:177], v[194:197], v[18:33]
	v_mov_b32_e32 v139, 0
	v_mov_b32_e32 v138, 0
	v_mov_b32_e32 v137, 0
	v_mov_b32_e32 v136, 0
	v_mov_b32_e32 v135, 0
	v_mfma_f32_32x32x16_f16 v[66:81], v[174:177], v[234:237], v[66:81]
	v_mov_b32_e32 v134, 0
	s_cbranch_scc1 .LBB15_21
	s_mul_i32 s6, s22, 0x206000
	s_add_u32 s6, s10, s6
	s_addc_u32 s7, s11, 0
	v_mov_b32_e32 v137, 0
	v_mov_b32_e32 v138, 0
	v_mov_b32_e32 v139, 0
	v_mov_b32_e32 v140, 0
	v_mov_b32_e32 v141, 0
	s_and_saveexec_b64 s[12:13], vcc
	s_cbranch_execz .LBB15_18
	v_ashrrev_i32_e32 v153, 31, v152
	v_lshl_add_u64 v[134:135], v[152:153], 4, s[6:7]
	global_load_dwordx4 v[138:141], v[134:135], off

.LBB15_21:
	s_mul_i32 s6, s23, 0x222
	v_subrev_u32_e32 v153, s6, v170
	v_mfma_f32_32x32x16_f16 v[66:81], v[250:253], v[194:197], v[66:81]
	s_and_b32 s7, s19, 1
	s_mulk_i32 s7, 0x6000
	v_mfma_f32_32x32x16_f16 v[2:17], v[174:177], v[238:241], v[2:17]
	v_lshrrev_b32_e32 v173, 2, v153
	s_and_b32 s6, s23, 1
	v_mfma_f32_32x32x16_f16 v[34:49], v[174:177], v[242:245], v[34:49]
	s_mul_i32 s23, s23, 0xffff7780
	s_add_i32 s7, s7, 0x13700
	v_mfma_f32_32x32x16_f16 v[34:49], v[250:253], v[238:241], v[34:49]
	v_bitop3_b32 v174, v173, v159, 3 bitop3:0x6c
	v_add_u32_e32 v234, s18, v171
	v_bitop3_b32 v173, v173, v160, 3 bitop3:0x6c
	s_mul_i32 s6, s6, 0x9b80
	v_add_u32_e32 v154, s23, v172
	v_lshl_or_b32 v155, v169, 4, s7
	v_lshl_add_u32 v174, v174, 4, v234
	v_lshl_add_u32 v173, v173, 4, v234
	v_add3_u32 v182, v174, s6, v154
	v_add3_u32 v173, v173, s6, v154
	v_add_u32_e32 v155, v155, v168
	ds_read_b128 v[174:177], v182
	ds_read_b128 v[178:181], v173
	ds_read_b128 v[182:185], v182 offset:2048
	ds_read_b128 v[186:189], v173 offset:2048
	ds_read_b128 v[190:193], v155
	v_lshl_or_b32 v173, v165, 4, s7
	v_add_u32_e32 v173, v173, v168
	ds_read_b128 v[194:197], v173
	s_waitcnt lgkmcnt(1)
	v_mfma_f32_32x32x16_f16 v[82:97], v[190:193], v[174:177], v[82:97]
	ds_read_b128 v[198:201], v155 offset:2048
	ds_read_b128 v[202:205], v173 offset:2048
	v_add_u32_e32 v206, 1, v153
	v_lshrrev_b32_e32 v210, 2, v206
	v_bitop3_b32 v206, v210, v159, 3 bitop3:0x6c
	v_bitop3_b32 v210, v210, v160, 3 bitop3:0x6c
	v_lshl_add_u32 v206, v206, 4, v234
	v_mfma_f32_32x32x16_f16 v[114:129], v[190:193], v[178:181], v[114:129]
	v_lshl_add_u32 v210, v210, 4, v234
	v_add3_u32 v214, v206, s6, v154
	v_add3_u32 v218, v210, s6, v154
	ds_read_b128 v[206:209], v214 offset:64
	ds_read_b128 v[210:213], v218 offset:64
	v_add_u32_e32 v153, 2, v153
	v_lshrrev_b32_e32 v153, 2, v153
	s_waitcnt lgkmcnt(4)
	v_mfma_f32_32x32x16_f16 v[114:129], v[194:197], v[174:177], v[114:129]
	ds_read_b128 v[214:217], v214 offset:2112
	ds_read_b128 v[218:221], v218 offset:2112
	s_add_i32 s19, s19, 1
	v_mfma_f32_32x32x16_f16 v[50:65], v[190:193], v[182:185], v[50:65]
	ds_read_b128 v[222:225], v155 offset:8192
	ds_read_b128 v[226:229], v173 offset:8192
	v_mfma_f32_32x32x16_f16 v[98:113], v[190:193], v[186:189], v[98:113]
	ds_read_b128 v[190:193], v155 offset:10240
	ds_read_b128 v[230:233], v173 offset:10240
	v_mfma_f32_32x32x16_f16 v[98:113], v[194:197], v[182:185], v[98:113]
	v_bitop3_b32 v194, v153, v159, 3 bitop3:0x6c
	v_bitop3_b32 v153, v153, v160, 3 bitop3:0x6c
	v_lshl_add_u32 v194, v194, 4, v234
	v_lshl_add_u32 v153, v153, 4, v234
	v_add3_u32 v238, v194, s6, v154
	v_add3_u32 v153, v153, s6, v154
	ds_read_b128 v[194:197], v238 offset:128
	ds_read_b128 v[234:237], v153 offset:128
	s_waitcnt lgkmcnt(11)
	v_mfma_f32_32x32x16_f16 v[18:33], v[198:201], v[174:177], v[18:33]
	ds_read_b128 v[238:241], v238 offset:2176
	ds_read_b128 v[242:245], v153 offset:2176
	s_and_b32 s6, s19, 1
	s_mul_i32 s12, s6, 0x6000
	s_add_i32 s12, s12, 0x13700
	v_lshl_add_u32 v153, v162, 4, s12
	v_mfma_f32_32x32x16_f16 v[66:81], v[198:201], v[178:181], v[66:81]
	ds_read_b128 v[178:181], v155 offset:16384
	ds_read_b128 v[246:249], v173 offset:16384
	s_waitcnt lgkmcnt(14)
	v_mfma_f32_32x32x16_f16 v[66:81], v[202:205], v[174:177], v[66:81]
	ds_read_b128 v[174:177], v155 offset:18432
	ds_read_b128 v[250:253], v173 offset:18432
	v_mfma_f32_32x32x16_f16 v[2:17], v[198:201], v[182:185], v[2:17]
	s_waitcnt vmcnt(1)
	ds_write_b128 v153, v[142:145]
	v_lshl_add_u32 v142, v163, 4, s12
	s_waitcnt vmcnt(0)
	ds_write_b128 v142, v[146:149]
	v_mfma_f32_32x32x16_f16 v[34:49], v[198:201], v[186:189], v[34:49]
	v_mfma_f32_32x32x16_f16 v[34:49], v[202:205], v[182:185], v[34:49]
	s_waitcnt lgkmcnt(13)
	v_mfma_f32_32x32x16_f16 v[82:97], v[222:225], v[206:209], v[82:97]
	v_mfma_f32_32x32x16_f16 v[114:129], v[222:225], v[210:213], v[114:129]
	s_waitcnt lgkmcnt(12)
	v_mfma_f32_32x32x16_f16 v[114:129], v[226:229], v[206:209], v[114:129]
	v_mfma_f32_32x32x16_f16 v[50:65], v[222:225], v[214:217], v[50:65]
	v_mfma_f32_32x32x16_f16 v[98:113], v[222:225], v[218:221], v[98:113]
	v_mfma_f32_32x32x16_f16 v[98:113], v[226:229], v[214:217], v[98:113]
	s_waitcnt lgkmcnt(11)
	v_mfma_f32_32x32x16_f16 v[18:33], v[190:193], v[206:209], v[18:33]
	v_mfma_f32_32x32x16_f16 v[66:81], v[190:193], v[210:213], v[66:81]
	s_waitcnt lgkmcnt(10)
	v_mfma_f32_32x32x16_f16 v[66:81], v[230:233], v[206:209], v[66:81]
	v_mfma_f32_32x32x16_f16 v[2:17], v[190:193], v[214:217], v[2:17]
	v_mfma_f32_32x32x16_f16 v[34:49], v[190:193], v[218:221], v[34:49]
	v_mfma_f32_32x32x16_f16 v[34:49], v[230:233], v[214:217], v[34:49]
	s_and_saveexec_b64 s[6:7], s[2:3]
	v_lshl_add_u32 v142, v164, 4, s12
	ds_write_b128 v142, v[130:133]
	s_or_b64 exec, exec, s[6:7]
	s_andn2_b64 vcc, exec, s[4:5]
	s_cbranch_vccnz .LBB15_12
	s_and_b32 s6, s22, 1
	s_mul_i32 s6, s6, 0x9b80
	v_cmp_gt_i32_e32 vcc, s21, v152
	v_lshrrev_b32_e32 v130, 4, v152
	s_and_saveexec_b64 s[4:5], vcc
	v_bitop3_b32 v131, v130, v152, 3 bitop3:0x6c
	v_lshl_add_u32 v131, v131, 4, s6
	ds_write_b128 v131, v[138:141]
	s_or_b64 exec, exec, s[4:5]
	v_add_u32_e32 v131, s20, v0
	v_cmp_gt_i32_e32 vcc, s21, v131
	s_and_saveexec_b64 s[4:5], vcc
	s_cbranch_execz .LBB15_11
	v_bitop3_b32 v130, v130, v131, 3 bitop3:0x6c
	v_lshl_add_u32 v130, v130, 4, s6
	ds_write_b128 v130, v[134:137]
	s_branch .LBB15_11
.LBB15_28:
	v_mfma_f32_32x32x16_f16 v[82:97], v[178:181], v[194:197], v[82:97]
	v_mfma_f32_32x32x16_f16 v[114:129], v[178:181], v[234:237], v[114:129]
	v_mfma_f32_32x32x16_f16 v[114:129], v[246:249], v[194:197], v[114:129]
	v_mfma_f32_32x32x16_f16 v[50:65], v[178:181], v[238:241], v[50:65]
	v_mfma_f32_32x32x16_f16 v[98:113], v[178:181], v[242:245], v[98:113]
	v_mfma_f32_32x32x16_f16 v[98:113], v[246:249], v[238:241], v[98:113]
	v_mfma_f32_32x32x16_f16 v[18:33], v[174:177], v[194:197], v[18:33]
	v_mfma_f32_32x32x16_f16 v[66:81], v[174:177], v[234:237], v[66:81]
	v_mfma_f32_32x32x16_f16 v[66:81], v[250:253], v[194:197], v[66:81]
	v_mfma_f32_32x32x16_f16 v[2:17], v[174:177], v[238:241], v[2:17]
	v_mfma_f32_32x32x16_f16 v[34:49], v[174:177], v[242:245], v[34:49]
	v_mfma_f32_32x32x16_f16 v[34:49], v[250:253], v[238:241], v[34:49]
	v_or_b32_e32 v154, v167, v166
	v_add_u32_e32 v130, 0x16c, v154
	v_lshrrev_b32_e32 v134, 2, v130
	v_lshlrev_b32_e32 v146, 4, v169
	v_bitop3_b32 v131, v134, v159, 3 bitop3:0x6c
	v_lshlrev_b32_e32 v135, 6, v130
	v_bitop3_b32 v134, v134, v160, 3 bitop3:0x6c
	s_mov_b32 s0, 0x13700
	v_lshl_or_b32 v138, v131, 4, v135
	v_lshl_or_b32 v142, v134, 4, v135
	v_add3_u32 v155, v168, v146, s0
	ds_read_b128 v[130:133], v138 offset:39808
	ds_read_b128 v[134:137], v142 offset:39808
	ds_read_b128 v[138:141], v138 offset:41856
	ds_read_b128 v[142:145], v142 offset:41856
	ds_read_b128 v[146:149], v155 offset:24576
	v_lshlrev_b32_e32 v150, 4, v165
	v_add3_u32 v214, v168, v150, s0
	ds_read_b128 v[150:153], v214 offset:24576
	s_waitcnt lgkmcnt(1)
	v_mfma_f32_32x32x16_f16 v[82:97], v[146:149], v[130:133], v[82:97]
	ds_read_b128 v[162:165], v155 offset:26624
	ds_read_b128 v[166:169], v214 offset:26624
	v_add_u32_e32 v170, 0x16d, v154
	v_lshrrev_b32_e32 v174, 2, v170
	v_bitop3_b32 v171, v174, v159, 3 bitop3:0x6c
	v_lshlrev_b32_e32 v175, 6, v170
	v_bitop3_b32 v174, v174, v160, 3 bitop3:0x6c
	v_mfma_f32_32x32x16_f16 v[114:129], v[146:149], v[134:137], v[114:129]
	v_lshl_or_b32 v178, v171, 4, v175
	v_lshl_or_b32 v182, v174, 4, v175
	ds_read_b128 v[170:173], v178 offset:39808
	ds_read_b128 v[174:177], v182 offset:39808
	v_add_u32_e32 v198, 0x16e, v154
	v_lshrrev_b32_e32 v199, 2, v198
	v_lshlrev_b32_e32 v198, 6, v198
	s_waitcnt lgkmcnt(4)
	v_mfma_f32_32x32x16_f16 v[114:129], v[150:153], v[130:133], v[114:129]
	ds_read_b128 v[178:181], v178 offset:41856
	ds_read_b128 v[182:185], v182 offset:41856
	s_or_b32 s6, s14, 0xb6
	s_mov_b32 s7, 0x1681682
	s_lshl_b32 s10, s15, 3
	s_mov_b32 s12, 0x80ae
	s_movk_i32 s13, 0xb5
	v_mfma_f32_32x32x16_f16 v[50:65], v[146:149], v[138:141], v[50:65]
	ds_read_b128 v[186:189], v155 offset:32768
	ds_read_b128 v[190:193], v214 offset:32768
	v_lshrrev_b32_e32 v1, 10, v1
	s_mov_b32 s11, 0
	v_mfma_f32_32x32x16_f16 v[98:113], v[146:149], v[142:145], v[98:113]
	ds_read_b128 v[146:149], v155 offset:34816
	ds_read_b128 v[194:197], v214 offset:34816
	v_mfma_f32_32x32x16_f16 v[98:113], v[150:153], v[138:141], v[98:113]
	v_bitop3_b32 v150, v199, v159, 3 bitop3:0x6c
	v_bitop3_b32 v199, v199, v160, 3 bitop3:0x6c
	v_lshl_or_b32 v202, v150, 4, v198
	v_lshl_or_b32 v206, v199, 4, v198
	ds_read_b128 v[150:153], v202 offset:39808
	ds_read_b128 v[198:201], v206 offset:39808
	s_waitcnt lgkmcnt(11)
	v_mfma_f32_32x32x16_f16 v[18:33], v[162:165], v[130:133], v[18:33]
	ds_read_b128 v[202:205], v202 offset:41856
	ds_read_b128 v[206:209], v206 offset:41856
	v_mfma_f32_32x32x16_f16 v[66:81], v[162:165], v[134:137], v[66:81]
	ds_read_b128 v[134:137], v155 offset:40960
	ds_read_b128 v[210:213], v214 offset:40960
	s_waitcnt lgkmcnt(14)
	v_mfma_f32_32x32x16_f16 v[66:81], v[166:169], v[130:133], v[66:81]
	ds_read_b128 v[130:133], v155 offset:43008
	ds_read_b128 v[214:217], v214 offset:43008
	s_waitcnt lgkmcnt(0)
	s_barrier
	s_barrier
	v_mfma_f32_32x32x16_f16 v[2:17], v[162:165], v[138:141], v[2:17]
	v_mfma_f32_32x32x16_f16 v[34:49], v[162:165], v[142:145], v[34:49]
	v_mfma_f32_32x32x16_f16 v[34:49], v[166:169], v[138:141], v[34:49]
	v_lshrrev_b32_e32 v139, 3, v0
	v_and_b32_e32 v140, 4, v0
	v_and_b32_e32 v138, 3, v0
	v_xor_b32_e32 v139, v139, v0
	v_cmp_eq_u32_e64 s[0:1], 0, v140
	v_and_b32_e32 v140, 7, v0
	v_add_u32_e32 v141, s6, v154
	v_mfma_f32_32x32x16_f16 v[82:97], v[186:189], v[170:173], v[82:97]
	v_mul_hi_u32 v142, v141, s7
	v_mul_u32_u24_e32 v142, 0xb6, v142
	v_lshlrev_b32_e32 v139, 4, v139
	v_sub_u32_e32 v142, v141, v142
	v_and_b32_e32 v139, 48, v139
	v_cmp_gt_u32_e32 vcc, s12, v141
	v_cmp_gt_u32_e64 s[4:5], s13, v142
	v_mfma_f32_32x32x16_f16 v[114:129], v[186:189], v[174:177], v[114:129]
	v_cmp_ne_u32_e64 s[2:3], 0, v142
	s_and_b64 s[4:5], vcc, s[4:5]
	s_and_b64 s[2:3], s[4:5], s[2:3]
	v_mfma_f32_32x32x16_f16 v[114:129], v[190:193], v[170:173], v[114:129]
	v_mfma_f32_32x32x16_f16 v[50:65], v[186:189], v[178:181], v[50:65]
	v_mfma_f32_32x32x16_f16 v[98:113], v[186:189], v[182:185], v[98:113]
	v_mfma_f32_32x32x16_f16 v[98:113], v[190:193], v[178:181], v[98:113]
	v_mfma_f32_32x32x16_f16 v[18:33], v[146:149], v[170:173], v[18:33]
	v_mfma_f32_32x32x16_f16 v[66:81], v[146:149], v[174:177], v[66:81]
	v_mfma_f32_32x32x16_f16 v[66:81], v[194:197], v[170:173], v[66:81]
	v_mfma_f32_32x32x16_f16 v[2:17], v[146:149], v[178:181], v[2:17]
	v_mfma_f32_32x32x16_f16 v[34:49], v[146:149], v[182:185], v[34:49]
	v_mfma_f32_32x32x16_f16 v[34:49], v[194:197], v[178:181], v[34:49]
	v_mfma_f32_32x32x16_f16 v[82:97], v[134:137], v[150:153], v[82:97]
	v_mfma_f32_32x32x16_f16 v[114:129], v[134:137], v[198:201], v[114:129]
	v_mfma_f32_32x32x16_f16 v[114:129], v[210:213], v[150:153], v[114:129]
	v_mfma_f32_32x32x16_f16 v[50:65], v[134:137], v[202:205], v[50:65]
	s_nop 10
	v_fmamk_f32 v84, v116, 0x3a000000, v84
	v_bitop3_b32 v116, v159, v0, 7 bitop3:0x78
	v_bitop3_b32 v0, v160, v0, 7 bitop3:0x78
	v_fmamk_f32 v86, v118, 0x3a000000, v86
	v_lshlrev_b32_e32 v118, 3, v0
	v_bitop3_b32 v0, v159, v140, 6 bitop3:0x36
	v_fmamk_f32 v87, v119, 0x3a000000, v87
	v_mfma_f32_32x32x16_f16 v[98:113], v[134:137], v[206:209], v[98:113]
	v_lshlrev_b32_e32 v119, 3, v0
	v_fmamk_f32 v0, v122, 0x3a000000, v90
	v_mul_f32_e32 v90, 0x3c800000, v0
	v_fmamk_f32 v0, v123, 0x3a000000, v91
	v_mul_f32_e32 v91, 0x3c800000, v0
	v_fmamk_f32 v0, v124, 0x3a000000, v92
	v_mul_f32_e32 v92, 0x3c800000, v0
	v_mfma_f32_32x32x16_f16 v[98:113], v[210:213], v[202:205], v[98:113]
	v_fmamk_f32 v0, v125, 0x3a000000, v93
	v_mul_f32_e32 v93, 0x3c800000, v0
	v_fmamk_f32 v0, v126, 0x3a000000, v94
	v_mul_f32_e32 v94, 0x3c800000, v0
	v_fmamk_f32 v0, v127, 0x3a000000, v95
	v_mul_f32_e32 v95, 0x3c800000, v0
	v_fmamk_f32 v0, v128, 0x3a000000, v96
	v_mfma_f32_32x32x16_f16 v[18:33], v[130:133], v[150:153], v[18:33]
	s_nop 3
	v_fmamk_f32 v50, v98, 0x3a000000, v50
	v_mul_f32_e32 v96, 0x3c800000, v0
	v_or_b32_e32 v0, 32, v154
	v_mul_f32_e32 v98, 0x3c800000, v50
	v_fmamk_f32 v50, v99, 0x3a000000, v51
	v_fmamk_f32 v88, v120, 0x3a000000, v88
	v_add_u32_e32 v120, s6, v0
	v_mfma_f32_32x32x16_f16 v[66:81], v[130:133], v[198:201], v[66:81]
	v_mul_f32_e32 v99, 0x3c800000, v50
	v_fmamk_f32 v50, v100, 0x3a000000, v52
	v_lshlrev_b32_e32 v100, 6, v0
	v_fmamk_f32 v0, v102, 0x3a000000, v54
	v_mul_f32_e32 v54, 0x3c800000, v0
	v_fmamk_f32 v0, v103, 0x3a000000, v55
	v_mul_f32_e32 v55, 0x3c800000, v0
	v_fmamk_f32 v0, v104, 0x3a000000, v56
	v_mul_f32_e32 v56, 0x3c800000, v0
	v_fmamk_f32 v0, v105, 0x3a000000, v57
	v_mfma_f32_32x32x16_f16 v[66:81], v[214:217], v[150:153], v[66:81]
	v_mul_f32_e32 v57, 0x3c800000, v0
	v_fmamk_f32 v0, v106, 0x3a000000, v58
	v_mul_f32_e32 v58, 0x3c800000, v0
	v_fmamk_f32 v0, v107, 0x3a000000, v59
	v_mul_f32_e32 v59, 0x3c800000, v0
	v_fmamk_f32 v0, v108, 0x3a000000, v60
	v_mul_f32_e32 v60, 0x3c800000, v0
	v_fmamk_f32 v0, v109, 0x3a000000, v61
	v_mul_f32_e32 v61, 0x3c800000, v0
	v_fmamk_f32 v0, v110, 0x3a000000, v62
	v_mul_f32_e32 v62, 0x3c800000, v0
	v_fmamk_f32 v0, v111, 0x3a000000, v63
	v_mul_f32_e32 v63, 0x3c800000, v0
	v_fmamk_f32 v0, v112, 0x3a000000, v64
	v_mfma_f32_32x32x16_f16 v[2:17], v[130:133], v[202:205], v[2:17]
	v_mul_f32_e32 v64, 0x3c800000, v0
	v_fmamk_f32 v0, v66, 0x3a000000, v18
	v_mul_f32_e32 v66, 0x3c800000, v0
	v_fmamk_f32 v0, v67, 0x3a000000, v19
	v_mul_f32_e32 v67, 0x3c800000, v0
	v_fmamk_f32 v0, v68, 0x3a000000, v20
	v_mul_f32_e32 v68, 0x3c800000, v0
	v_mfma_f32_32x32x16_f16 v[34:49], v[130:133], v[206:209], v[34:49]
	v_fmamk_f32 v0, v69, 0x3a000000, v21
	v_mul_f32_e32 v69, 0x3c800000, v0
	v_fmamk_f32 v0, v70, 0x3a000000, v22
	v_mul_f32_e32 v70, 0x3c800000, v0
	v_fmamk_f32 v0, v71, 0x3a000000, v23
	v_mul_f32_e32 v71, 0x3c800000, v0
	v_fmamk_f32 v0, v72, 0x3a000000, v24
	v_mul_f32_e32 v72, 0x3c800000, v0
	v_fmamk_f32 v0, v73, 0x3a000000, v25
	v_mfma_f32_32x32x16_f16 v[34:49], v[214:217], v[202:205], v[34:49]
	v_mul_f32_e32 v73, 0x3c800000, v0
	v_fmamk_f32 v0, v74, 0x3a000000, v26
	v_mul_f32_e32 v74, 0x3c800000, v0
	v_fmamk_f32 v0, v75, 0x3a000000, v27
	v_mul_f32_e32 v75, 0x3c800000, v0
	v_fmamk_f32 v0, v76, 0x3a000000, v28
	v_mul_f32_e32 v76, 0x3c800000, v0
	v_fmamk_f32 v0, v77, 0x3a000000, v29
	v_mul_f32_e32 v77, 0x3c800000, v0
	v_fmamk_f32 v0, v78, 0x3a000000, v30
	v_mul_f32_e32 v78, 0x3c800000, v0
	v_fmamk_f32 v0, v79, 0x3a000000, v31
	v_mul_f32_e32 v79, 0x3c800000, v0
	v_fmamk_f32 v0, v80, 0x3a000000, v32
	v_mul_f32_e32 v80, 0x3c800000, v0
	v_fmamk_f32 v0, v34, 0x3a000000, v2
	v_mul_f32_e32 v52, 0x3c800000, v50
	v_fmamk_f32 v50, v101, 0x3a000000, v53
	v_mul_f32_e32 v101, 0x3c800000, v0
	v_fmamk_f32 v0, v35, 0x3a000000, v3
	v_mul_f32_e32 v102, 0x3c800000, v0
	v_fmamk_f32 v0, v36, 0x3a000000, v4
	v_mul_f32_e32 v103, 0x3c800000, v0
	v_fmamk_f32 v0, v37, 0x3a000000, v5
	v_mul_f32_e32 v104, 0x3c800000, v0
	v_fmamk_f32 v0, v38, 0x3a000000, v6
	v_mul_f32_e32 v105, 0x3c800000, v0
	v_fmamk_f32 v0, v39, 0x3a000000, v7
	v_mul_f32_e32 v106, 0x3c800000, v0
	v_fmamk_f32 v0, v40, 0x3a000000, v8
	v_mul_f32_e32 v107, 0x3c800000, v0
	v_fmamk_f32 v0, v41, 0x3a000000, v9
	v_mul_f32_e32 v108, 0x3c800000, v0
	v_fmamk_f32 v0, v42, 0x3a000000, v10
	v_mul_f32_e32 v109, 0x3c800000, v0
	v_fmamk_f32 v0, v43, 0x3a000000, v11
	v_mul_f32_e32 v110, 0x3c800000, v0
	v_fmamk_f32 v0, v44, 0x3a000000, v12
	v_mul_f32_e32 v111, 0x3c800000, v0
	v_fmamk_f32 v0, v45, 0x3a000000, v13
	v_fmamk_f32 v89, v121, 0x3a000000, v89
	v_mul_hi_u32 v121, v120, s7
	v_mul_f32_e32 v112, 0x3c800000, v0
	v_fmamk_f32 v0, v46, 0x3a000000, v14
	v_or_b32_e32 v2, 0x80, v158
	v_mul_u32_u24_e32 v121, 0xb6, v121
	v_fmac_f32_e32 v65, 0x3a000000, v113
	v_mul_f32_e32 v113, 0x3c800000, v0
	v_fmamk_f32 v0, v47, 0x3a000000, v15
	v_lshlrev_b32_e32 v4, 6, v2
	v_lshlrev_b32_e32 v5, 4, v138
	v_add_u32_e32 v2, s14, v2
	v_or_b32_e32 v124, s10, v1
	v_lshlrev_b32_e32 v1, 14, v1
	v_sub_u32_e32 v121, v120, v121
	v_cmp_gt_u32_e32 vcc, s12, v120
	v_mul_f32_e32 v120, 0x3c800000, v0
	v_fmamk_f32 v0, v48, 0x3a000000, v16
	v_lshl_or_b32 v2, v2, 6, v5
	v_or3_b32 v125, v1, v4, v139
	v_add_u32_e32 v1, s14, v158
	v_cmp_ne_u32_e64 s[4:5], 0, v121
	v_cmp_gt_u32_e64 s[6:7], s13, v121
	v_mul_f32_e32 v121, 0x3c800000, v0
	v_lshrrev_b32_e32 v0, 2, v157
	v_add_u32_e32 v2, 0x2f80, v2
	v_mov_b32_e32 v3, 0
	v_lshl_or_b32 v1, v1, 6, v5
	v_lshl_add_u64 v[24:25], s[8:9], 0, v[2:3]
	v_add_u32_e32 v2, 0x2f80, v1
	v_add_u32_e32 v1, s14, v0
	v_fmamk_f32 v82, v114, 0x3a000000, v82
	v_lshlrev_b32_e32 v114, 2, v161
	v_lshl_or_b32 v1, v1, 6, v5
	v_lshl_or_b32 v114, v159, 4, v114
	v_fmamk_f32 v83, v115, 0x3a000000, v83
	v_fmamk_f32 v85, v117, 0x3a000000, v85
	v_bitop3_b32 v117, v159, v140, 4 bitop3:0x36
	v_fmac_f32_e32 v97, 0x3a000000, v129
	s_and_b64 s[6:7], vcc, s[6:7]
	v_fmac_f32_e32 v33, 0x3a000000, v81
	v_fmac_f32_e32 v17, 0x3a000000, v49
	v_lshl_add_u64 v[26:27], s[8:9], 0, v[2:3]
	v_add_u32_e32 v2, 0x2f80, v1
	v_mul_f32_e32 v82, 0x3c800000, v82
	v_add_u32_e32 v114, 0x1f700, v114
	v_mul_f32_e32 v83, 0x3c800000, v83
	v_mul_f32_e32 v84, 0x3c800000, v84
	v_mul_f32_e32 v85, 0x3c800000, v85
	v_lshlrev_b32_e32 v115, 6, v154
	v_lshlrev_b32_e32 v116, 3, v116
	v_lshlrev_b32_e32 v117, 3, v117
	v_mul_f32_e32 v86, 0x3c800000, v86
	v_mul_f32_e32 v87, 0x3c800000, v87
	v_mul_f32_e32 v88, 0x3c800000, v88
	v_mul_f32_e32 v89, 0x3c800000, v89
	v_mul_f32_e32 v97, 0x3c800000, v97
	s_and_b64 s[4:5], s[6:7], s[4:5]
	v_mul_f32_e32 v53, 0x3c800000, v50
	v_mul_f32_e32 v65, 0x3c800000, v65
	v_mul_f32_e32 v81, 0x3c800000, v33
	v_mul_f32_e32 v122, 0x3c800000, v17
	v_lshl_or_b32 v123, v158, 6, v139
	v_lshl_add_u64 v[28:29], s[8:9], 0, v[2:3]
	v_mov_b32_e32 v126, s10
	v_lshl_or_b32 v127, v0, 6, v139
	s_mov_b64 s[6:7], -1
	s_mov_b32 s12, 0x38800000
	s_mov_b32 s13, 0x206000
	v_mov_b32_e32 v128, 0x206000

amdhsa.kernels:
  - .agpr_count:     0
    .args:
      - .actual_access:  read_only
        .address_space:  global
        .offset:         0
        .size:           8
        .value_kind:     global_buffer
      - .actual_access:  write_only
        .address_space:  global
        .offset:         8
        .size:           8
        .value_kind:     global_buffer
    .group_segment_fixed_size: 0
    .kernarg_segment_align: 8
    .kernarg_segment_size: 16
    .language:       OpenCL C
    .language_version:
      - 2
      - 0
    .max_flat_workgroup_size: 256
    .name:           _Z13prep_x_kernelPKfP15HIP_vector_typeIjLj4EE
    .private_segment_fixed_size: 0
    .sgpr_count:     23
    .sgpr_spill_count: 0
    .symbol:         _Z13prep_x_kernelPKfP15HIP_vector_typeIjLj4EE.kd
    .uniform_work_group_size: 1
    .uses_dynamic_stack: false
    .vgpr_count:     36
    .vgpr_spill_count: 0
    .wavefront_size: 64
  - .agpr_count:     0
    .args:
      - .actual_access:  read_only
        .address_space:  global
        .offset:         0
        .size:           8
        .value_kind:     global_buffer
      - .actual_access:  write_only
        .address_space:  global
        .offset:         8
        .size:           8
        .value_kind:     global_buffer
      - .offset:         16
        .size:           4
        .value_kind:     by_value
      - .offset:         20
        .size:           4
        .value_kind:     by_value
      - .offset:         24
        .size:           4
        .value_kind:     by_value
      - .offset:         28
        .size:           4
        .value_kind:     by_value
    .group_segment_fixed_size: 0
    .kernarg_segment_align: 8
    .kernarg_segment_size: 32
    .language:       OpenCL C
    .language_version:
      - 2
      - 0
    .max_flat_workgroup_size: 256
    .name:           _Z13prep_w_kernelPKfP15HIP_vector_typeIjLj4EEiiii
    .private_segment_fixed_size: 0
    .sgpr_count:     15
    .sgpr_spill_count: 0
    .symbol:         _Z13prep_w_kernelPKfP15HIP_vector_typeIjLj4EEiiii.kd
    .uniform_work_group_size: 1
    .uses_dynamic_stack: false
    .vgpr_count:     34
    .vgpr_spill_count: 0
    .wavefront_size: 64
  - .agpr_count:     0
    .args:
      - .actual_access:  write_only
        .address_space:  global
        .offset:         0
        .size:           8
        .value_kind:     global_buffer
    .group_segment_fixed_size: 0
    .kernarg_segment_align: 8
    .kernarg_segment_size: 8
    .language:       OpenCL C
    .language_version:
      - 2
      - 0
    .max_flat_workgroup_size: 256
    .name:           _Z18zero_border_kernelP15HIP_vector_typeIjLj4EE
    .private_segment_fixed_size: 0
    .sgpr_count:     12
    .sgpr_spill_count: 0
    .symbol:         _Z18zero_border_kernelP15HIP_vector_typeIjLj4EE.kd
    .uniform_work_group_size: 1
    .uses_dynamic_stack: false
    .vgpr_count:     6
    .vgpr_spill_count: 0
    .wavefront_size: 64
  - .agpr_count:     0
    .args:
      - .actual_access:  read_only
        .address_space:  global
        .offset:         0
        .size:           8
        .value_kind:     global_buffer
      - .address_space:  global
        .offset:         8
        .size:           8
        .value_kind:     global_buffer
      - .actual_access:  read_only
        .address_space:  global
        .offset:         16
        .size:           8
        .value_kind:     global_buffer
      - .actual_access:  read_only
        .address_space:  global
        .offset:         24
        .size:           8
        .value_kind:     global_buffer
      - .actual_access:  read_only
        .address_space:  global
        .offset:         32
        .size:           8
        .value_kind:     global_buffer
      - .actual_access:  write_only
        .address_space:  global
        .offset:         40
        .size:           8
        .value_kind:     global_buffer
    .group_segment_fixed_size: 154880
    .kernarg_segment_align: 8
    .kernarg_segment_size: 48
    .language:       OpenCL C
    .language_version:
      - 2
      - 0
    .max_flat_workgroup_size: 512
    .name:           _Z12conv1_kernelPKfPK15HIP_vector_typeIjLj4EES0_S0_S0_PDF16_
    .private_segment_fixed_size: 0
    .sgpr_count:     46
    .sgpr_spill_count: 0
    .symbol:         _Z12conv1_kernelPKfPK15HIP_vector_typeIjLj4EES0_S0_S0_PDF16_.kd
    .uniform_work_group_size: 1
    .uses_dynamic_stack: false
    .vgpr_count:     256
    .vgpr_spill_count: 0
    .wavefront_size: 64
  - .agpr_count:     0
    .args:
      - .actual_access:  read_only
        .address_space:  global
        .offset:         0
        .size:           8
        .value_kind:     global_buffer
      - .actual_access:  read_only
        .address_space:  global
        .offset:         8
        .size:           8
        .value_kind:     global_buffer
      - .actual_access:  read_only
        .address_space:  global
        .offset:         16
        .size:           8
        .value_kind:     global_buffer
      - .actual_access:  write_only
        .address_space:  global
        .offset:         24
        .size:           8
        .value_kind:     global_buffer
      - .actual_access:  write_only
        .address_space:  global
        .offset:         32
        .size:           8
        .value_kind:     global_buffer
    .group_segment_fixed_size: 116480
    .kernarg_segment_align: 8
    .kernarg_segment_size: 40
    .language:       OpenCL C
    .language_version:
      - 2
      - 0
    .max_flat_workgroup_size: 512
    .name:           _Z12conv3_kernelPK15HIP_vector_typeIjLj4EES2_PKfPfS5_
    .private_segment_fixed_size: 0
    .sgpr_count:     22
    .sgpr_spill_count: 0
    .symbol:         _Z12conv3_kernelPK15HIP_vector_typeIjLj4EES2_PKfPfS5_.kd
    .uniform_work_group_size: 1
    .uses_dynamic_stack: false
    .vgpr_count:     122
    .vgpr_spill_count: 0
    .wavefront_size: 64
  - .agpr_count:     0
    .args:
      - .actual_access:  read_only
        .address_space:  global
        .offset:         0
        .size:           8
        .value_kind:     global_buffer
      - .actual_access:  read_only
        .address_space:  global
        .offset:         8
        .size:           8
        .value_kind:     global_buffer
      - .actual_access:  write_only
        .address_space:  global
        .offset:         16
        .size:           8
        .value_kind:     global_buffer
      - .address_space:  global
        .offset:         24
        .size:           8
        .value_kind:     global_buffer
    .group_segment_fixed_size: 32768
    .kernarg_segment_align: 8
    .kernarg_segment_size: 32
    .language:       OpenCL C
    .language_version:
      - 2
      - 0
    .max_flat_workgroup_size: 256
    .name:           _Z15nms_hist_kernelPKfS0_PjS1_
    .private_segment_fixed_size: 0
    .sgpr_count:     102
    .sgpr_spill_count: 0
    .symbol:         _Z15nms_hist_kernelPKfS0_PjS1_.kd
    .uniform_work_group_size: 1
    .uses_dynamic_stack: false
    .vgpr_count:     128
    .vgpr_spill_count: 0
    .wavefront_size: 64
  - .agpr_count:     0
    .args:
      - .actual_access:  read_only
        .address_space:  global
        .offset:         0
        .size:           8
        .value_kind:     global_buffer
      - .actual_access:  write_only
        .address_space:  global
        .offset:         8
        .size:           8
        .value_kind:     global_buffer
    .group_segment_fixed_size: 4096
    .kernarg_segment_align: 8
    .kernarg_segment_size: 16
    .language:       OpenCL C
    .language_version:
      - 2
      - 0
    .max_flat_workgroup_size: 1024
    .name:           _Z17select_bin_kernelPKjPi
    .private_segment_fixed_size: 0
    .sgpr_count:     23
    .sgpr_spill_count: 0
    .symbol:         _Z17select_bin_kernelPKjPi.kd
    .uniform_work_group_size: 1
    .uses_dynamic_stack: false
    .vgpr_count:     13
    .vgpr_spill_count: 0
    .wavefront_size: 64
  - .agpr_count:     0
    .args:
      - .actual_access:  read_only
        .address_space:  global
        .offset:         0
        .size:           8
        .value_kind:     global_buffer
      - .actual_access:  read_only
        .address_space:  global
        .offset:         8
        .size:           8
        .value_kind:     global_buffer
      - .address_space:  global
        .offset:         16
        .size:           8
        .value_kind:     global_buffer
      - .actual_access:  write_only
        .address_space:  global
        .offset:         24
        .size:           8
        .value_kind:     global_buffer
    .group_segment_fixed_size: 2052
    .kernarg_segment_align: 8
    .kernarg_segment_size: 32
    .language:       OpenCL C
    .language_version:
      - 2
      - 0
    .max_flat_workgroup_size: 512
    .name:           _Z14collect_kernelPKjS0_PiS1_
    .private_segment_fixed_size: 0
    .sgpr_count:     70
    .sgpr_spill_count: 0
    .symbol:         _Z14collect_kernelPKjS0_PiS1_.kd
    .uniform_work_group_size: 1
    .uses_dynamic_stack: false
    .vgpr_count:     34
    .vgpr_spill_count: 0
    .wavefront_size: 64
  - .agpr_count:     0
    .args:
      - .actual_access:  read_only
        .address_space:  global
        .offset:         0
        .size:           8
        .value_kind:     global_buffer
      - .actual_access:  read_only
        .address_space:  global
        .offset:         8
        .size:           8
        .value_kind:     global_buffer
      - .actual_access:  read_only
        .address_space:  global
        .offset:         16
        .size:           8
        .value_kind:     global_buffer
      - .actual_access:  read_only
        .address_space:  global
        .offset:         24
        .size:           8
        .value_kind:     global_buffer
      - .actual_access:  write_only
        .address_space:  global
        .offset:         32
        .size:           8
        .value_kind:     global_buffer
    .group_segment_fixed_size: 49664
    .kernarg_segment_align: 8
    .kernarg_segment_size: 40
    .language:       OpenCL C
    .language_version:
      - 2
      - 0
    .max_flat_workgroup_size: 1024
    .name:           _Z11rank_kernelPKfS0_PKiS2_Pi
    .private_segment_fixed_size: 0
    .sgpr_count:     23
    .sgpr_spill_count: 0
    .symbol:         _Z11rank_kernelPKfS0_PKiS2_Pi.kd
    .uniform_work_group_size: 1
    .uses_dynamic_stack: false
    .vgpr_count:     12
    .vgpr_spill_count: 0
    .wavefront_size: 64
  - .agpr_count:     0
    .args:
      - .actual_access:  read_only
        .address_space:  global
        .offset:         0
        .size:           8
        .value_kind:     global_buffer
      - .actual_access:  read_only
        .address_space:  global
        .offset:         8
        .size:           8
        .value_kind:     global_buffer
      - .actual_access:  write_only
        .address_space:  global
        .offset:         16
        .size:           8
        .value_kind:     global_buffer
      - .actual_access:  write_only
        .address_space:  global
        .offset:         24
        .size:           8
        .value_kind:     global_buffer
    .group_segment_fixed_size: 0
    .kernarg_segment_align: 8
    .kernarg_segment_size: 32
    .language:       OpenCL C
    .language_version:
      - 2
      - 0
    .max_flat_workgroup_size: 256
    .name:           _Z15prep_kvw_kernelPKfS0_PDF16_S1_
    .private_segment_fixed_size: 0
    .sgpr_count:     14
    .sgpr_spill_count: 0
    .symbol:         _Z15prep_kvw_kernelPKfS0_PDF16_S1_.kd
    .uniform_work_group_size: 1
    .uses_dynamic_stack: false
    .vgpr_count:     7
    .vgpr_spill_count: 0
    .wavefront_size: 64
  - .agpr_count:     0
    .args:
      - .actual_access:  read_only
        .address_space:  global
        .offset:         0
        .size:           8
        .value_kind:     global_buffer
      - .actual_access:  read_only
        .address_space:  global
        .offset:         8
        .size:           8
        .value_kind:     global_buffer
      - .actual_access:  read_only
        .address_space:  global
        .offset:         16
        .size:           8
        .value_kind:     global_buffer
      - .actual_access:  read_only
        .address_space:  global
        .offset:         24
        .size:           8
        .value_kind:     global_buffer
      - .actual_access:  write_only
        .address_space:  global
        .offset:         32
        .size:           8
        .value_kind:     global_buffer
    .group_segment_fixed_size: 67856
    .kernarg_segment_align: 8
    .kernarg_segment_size: 40
    .language:       OpenCL C
    .language_version:
      - 2
      - 0
    .max_flat_workgroup_size: 448
    .name:           _Z17cross_attn_kernelPKDF16_S0_S0_S0_Pf
    .private_segment_fixed_size: 0
    .sgpr_count:     26
    .sgpr_spill_count: 0
    .symbol:         _Z17cross_attn_kernelPKDF16_S0_S0_S0_Pf.kd
    .uniform_work_group_size: 1
    .uses_dynamic_stack: false
    .vgpr_count:     74
    .vgpr_spill_count: 0
    .wavefront_size: 64
  - .agpr_count:     0
    .args:
      - .offset:         0
        .size:           424
        .value_kind:     by_value
      - .offset:         424
        .size:           88
        .value_kind:     by_value
    .group_segment_fixed_size: 137216
    .kernarg_segment_align: 8
    .kernarg_segment_size: 512
    .language:       OpenCL C
    .language_version:
      - 2
      - 0
    .max_flat_workgroup_size: 512
    .name:           _Z12tailA_kernel5TailP3KvP
    .private_segment_fixed_size: 0
    .sgpr_count:     44
    .sgpr_spill_count: 0
    .symbol:         _Z12tailA_kernel5TailP3KvP.kd
    .uniform_work_group_size: 1
    .uses_dynamic_stack: false
    .vgpr_count:     200
    .vgpr_spill_count: 0
    .wavefront_size: 64
  - .agpr_count:     0
    .args:
      - .offset:         0
        .size:           424
        .value_kind:     by_value
      - .offset:         424
        .size:           88
        .value_kind:     by_value
    .group_segment_fixed_size: 146592
    .kernarg_segment_align: 8
    .kernarg_segment_size: 512
    .language:       OpenCL C
    .language_version:
      - 2
      - 0
    .max_flat_workgroup_size: 512
    .name:           _Z12tailB_kernel5TailP3KvP
    .private_segment_fixed_size: 0
    .sgpr_count:     44
    .sgpr_spill_count: 0
    .symbol:         _Z12tailB_kernel5TailP3KvP.kd
    .uniform_work_group_size: 1
    .uses_dynamic_stack: false
    .vgpr_count:     216
    .vgpr_spill_count: 0
    .wavefront_size: 64
  - .agpr_count:     0
    .args:
      - .offset:         0
        .size:           424
        .value_kind:     by_value
    .group_segment_fixed_size: 36896
    .kernarg_segment_align: 8
    .kernarg_segment_size: 424
    .language:       OpenCL C
    .language_version:
      - 2
      - 0
    .max_flat_workgroup_size: 512
    .name:           _Z12tailC_kernel5TailP
    .private_segment_fixed_size: 0
    .sgpr_count:     58
    .sgpr_spill_count: 0
    .symbol:         _Z12tailC_kernel5TailP.kd
    .uniform_work_group_size: 1
    .uses_dynamic_stack: false
    .vgpr_count:     113
    .vgpr_spill_count: 0
    .wavefront_size: 64
  - .agpr_count:     0
    .args:
      - .offset:         0
        .size:           344
        .value_kind:     by_value
    .group_segment_fixed_size: 0
    .kernarg_segment_align: 8
    .kernarg_segment_size: 344
    .language:       OpenCL C
    .language_version:
      - 2
      - 0
    .max_flat_workgroup_size: 256
    .name:           _Z15prep_all_kernel5PrepP
    .private_segment_fixed_size: 0
    .sgpr_count:     31
    .sgpr_spill_count: 0
    .symbol:         _Z15prep_all_kernel5PrepP.kd
    .uniform_work_group_size: 1
    .uses_dynamic_stack: false
    .vgpr_count:     39
    .vgpr_spill_count: 0
    .wavefront_size: 64
  - .agpr_count:     0
    .args:
      - .actual_access:  read_only
        .address_space:  global
        .offset:         0
        .size:           8
        .value_kind:     global_buffer
      - .actual_access:  read_only
        .address_space:  global
        .offset:         8
        .size:           8
        .value_kind:     global_buffer
      - .actual_access:  read_only
        .address_space:  global
        .offset:         16
        .size:           8
        .value_kind:     global_buffer
      - .actual_access:  read_only
        .address_space:  global
        .offset:         24
        .size:           8
        .value_kind:     global_buffer
      - .actual_access:  read_only
        .address_space:  global
        .offset:         32
        .size:           8
        .value_kind:     global_buffer
      - .actual_access:  write_only
        .address_space:  global
        .offset:         40
        .size:           8
        .value_kind:     global_buffer
      - .actual_access:  read_only
        .address_space:  global
        .offset:         48
        .size:           8
        .value_kind:     global_buffer
      - .actual_access:  read_only
        .address_space:  global
        .offset:         56
        .size:           8
        .value_kind:     global_buffer
    .group_segment_fixed_size: 130304
    .kernarg_segment_align: 8
    .kernarg_segment_size: 64
    .language:       OpenCL C
    .language_version:
      - 2
      - 0
    .max_flat_workgroup_size: 512
    .name:           _Z11conv_kernelILi8ELi128ELi0EEvPK15HIP_vector_typeIjLj4EES3_PKfS5_S5_PDF16_PfS7_
    .private_segment_fixed_size: 0
    .sgpr_count:     30
    .sgpr_spill_count: 0
    .symbol:         _Z11conv_kernelILi8ELi128ELi0EEvPK15HIP_vector_typeIjLj4EES3_PKfS5_S5_PDF16_PfS7_.kd
    .uniform_work_group_size: 1
    .uses_dynamic_stack: false
    .vgpr_count:     254
    .vgpr_spill_count: 0
    .wavefront_size: 64
